# baseline (speedup 1.0000x reference)
_Z6k_gemm8GemmProbS_:
	s_movk_i32 s3, 0xe0
	s_add_u32 s6, s0, 48
	s_addc_u32 s7, s1, 0
	v_lshrrev_b32_e32 v3, 6, v0
	v_bfe_u32 v2, v0, 3, 3
	s_waitcnt lgkmcnt(0)
	s_cmp_lt_i32 s2, s3
	s_cselect_b64 s[60:61], -1, 0
	s_and_b64 s[4:5], s[60:61], exec
	s_cselect_b32 s3, 0, s3
	s_cselect_b32 s5, s1, s7
	s_cselect_b32 s4, s0, s6
	s_sub_i32 s10, s2, s3
	s_mul_i32 s3, s10, 0xe0
	v_lshl_or_b32 v2, v3, 3, v2
	v_lshrrev_b32_e32 v4, 1, v2
	v_add_u32_e32 v10, s3, v2
	s_load_dwordx8 s[52:59], s[4:5], 0x0
	s_load_dword s8, s[4:5], 0x28
	v_xor_b32_e32 v4, v4, v0
	v_min_i32_e32 v5, 0xc34f, v10
	v_lshlrev_b32_e32 v126, 6, v5
	v_lshlrev_b32_e32 v4, 3, v4
	v_add_u32_e32 v5, 0x80, v10
	v_bfe_u32 v127, v0, 6, 2
	v_and_b32_e32 v1, 15, v0
	v_and_b32_e32 v132, 56, v4
	v_add_u32_e32 v4, 64, v10
	v_min_i32_e32 v5, 0xc34f, v5
	v_lshlrev_b32_e32 v134, 6, v127
	v_min_i32_e32 v4, 0xc34f, v4
	v_lshlrev_b32_e32 v130, 6, v5
	v_or_b32_e32 v5, v134, v1
	v_lshl_add_u32 v139, v3, 10, 0
	v_or_b32_e32 v118, v132, v126
	v_lshlrev_b32_e32 v128, 6, v4
	v_lshlrev_b32_e32 v5, 2, v5
	v_mov_b32_e32 v119, 0
	v_readfirstlane_b32 s6, v139
	v_add_u32_e32 v3, 0x2000, v139
	v_or_b32_e32 v4, v132, v128
	s_waitcnt lgkmcnt(0)
	global_load_dword v117, v5, s[56:57]
	global_load_dword v116, v5, s[56:57] offset:64
	global_load_dword v115, v5, s[56:57] offset:128
	global_load_dword v114, v5, s[56:57] offset:192
	v_lshl_add_u64 v[8:9], v[118:119], 1, s[52:53]
	s_mov_b32 m0, s6
	v_mov_b32_e32 v5, v119
	v_readfirstlane_b32 s6, v3
	v_add_u32_e32 v3, 0x4000, v139
	v_or_b32_e32 v6, v132, v130
	global_load_lds_dwordx4 v[8:9], off nt
	v_lshl_add_u64 v[4:5], v[4:5], 1, s[52:53]
	s_mov_b32 m0, s6
	v_mov_b32_e32 v7, v119
	v_readfirstlane_b32 s6, v3
	global_load_lds_dwordx4 v[4:5], off nt
	v_lshl_add_u64 v[4:5], v[6:7], 1, s[52:53]
	s_mov_b32 m0, s6
	global_load_lds_dwordx4 v[4:5], off nt
	v_add_u32_e32 v3, 0xc0, v10
	v_min_i32_e32 v3, 0xc34f, v3
	s_movk_i32 s4, 0x100
	v_lshlrev_b32_e32 v133, 6, v3
	v_cmp_gt_u32_e64 s[4:5], s4, v0
	s_and_saveexec_b64 s[6:7], s[4:5]
	s_cbranch_execz .LBB5_2
	v_add_u32_e32 v3, 0x6000, v139
	v_or_b32_e32 v118, v132, v133
	v_readfirstlane_b32 s9, v3
	v_lshl_add_u64 v[4:5], v[118:119], 1, s[52:53]
	s_mov_b32 m0, s9
	s_nop 0
	global_load_lds_dwordx4 v[4:5], off nt
